# prologue x/mem row conversion: the row's four loads issued together behind counted waits instead of one load + vmcnt(0) per chunk
# baseline (speedup 1.0000x reference)
; #define GAS __attribute__((address_space(1)))
; __device__ __forceinline__ unsigned pk2(float lo, float hi) { return f2bf(lo) | (f2bf(hi) << 16); }
; __device__ __forceinline__ float bf2f_lo(unsigned w) { return __uint_as_float(w << 16); }
; __device__ __forceinline__ float bf2f_hi(unsigned w) { return __uint_as_float(w & 0xffff0000u); }
; __device__ __forceinline__ void p0_prologue(Frame& F, KArgs A) {
;     ...
;     for (int m = gw; m < M + 1024; m += NGW) {
;         const bool ismem = m >= M; const int row = ismem ? m - M : m;
;         const GAS f32x4* xr = (const GAS f32x4*)((ismem ? INF(A, I_MEM) : INF(A, I_X)) + (size_t)row * D) + lane;
;         GAS unsigned long long* o8 = (GAS unsigned long long*)((bf16*)(ws + (ismem ? WS_MK : WS_X)) + (size_t)row * D) + lane;
;         float s = 0.f;
; #pragma unroll
;         for (int j = 0; j < 4; ++j) { const f32x4 v = xr[64 * j]; const unsigned a = pk2(v.x, v.y), b = pk2(v.z, v.w); o8[64 * j] = (unsigned long long)a | ((unsigned long long)b << 32);
;             s += (bf2f_lo(a) * bf2f_lo(a) + bf2f_hi(a) * bf2f_hi(a)) + (bf2f_lo(b) * bf2f_lo(b) + bf2f_hi(b) * bf2f_hi(b)); }
;         s = wave_sum(s);
;         if (ismem) { if (lane == 0) ((float*)(ws + WS_MSS))[row] = s; } else if (lane < 16) ((float*)(ws + WS_SS))[(size_t)row * 16 + lane] = lane == 0 ? s : 0.f;
;     }
.LBB0_355:
	s_add_i32 s8, s3, 0xffff8000
	s_cmpk_gt_i32 s3, 0x7fff
	s_cselect_b32 s9, 8, 0
	s_cselect_b32 s8, s8, s3
	s_cselect_b32 s22, s21, 0x7a00000
	s_add_u32 s10, s14, s9
	s_addc_u32 s11, s15, 0
	s_load_dwordx2 s[10:11], s[10:11], 0x0
	s_ashr_i32 s9, s8, 31
	s_lshl_b64 s[16:17], s[8:9], 12
	s_waitcnt lgkmcnt(0)
	s_add_u32 s16, s10, s16
	s_addc_u32 s17, s11, s17
	global_load_dwordx4 v[14:17], v13, s[16:17]
	global_load_dwordx4 v[32:35], v13, s[16:17] offset:1024
	global_load_dwordx4 v[36:39], v13, s[16:17] offset:2048
	global_load_dwordx4 v[40:43], v13, s[16:17] offset:3072
	s_add_u32 s22, s12, s22
	s_addc_u32 s23, s13, 0
	s_lshl_b64 s[10:11], s[8:9], 11
	s_add_u32 s10, s22, s10
	s_addc_u32 s11, s23, s11
	s_cmp_lt_i32 s3, 0x8000
	s_waitcnt vmcnt(3)
	v_bfe_u32 v18, v14, 16, 1
	v_bfe_u32 v19, v15, 16, 1
	v_bfe_u32 v21, v17, 16, 1
	v_bfe_u32 v20, v16, 16, 1
	v_add3_u32 v18, v14, v18, s20
	v_add3_u32 v14, v15, v19, s20
	v_add3_u32 v15, v17, v21, s20
	v_add3_u32 v19, v16, v20, s20
	v_and_b32_e32 v20, 0xffff0000, v14
	v_and_b32_e32 v21, 0xffff0000, v15
	v_or_b32_sdwa v14, v20, v18 dst_sel:DWORD dst_unused:UNUSED_PAD src0_sel:DWORD src1_sel:WORD_1
	v_or_b32_sdwa v15, v21, v19 dst_sel:DWORD dst_unused:UNUSED_PAD src0_sel:DWORD src1_sel:WORD_1
	global_store_dwordx2 v2, v[14:15], s[10:11]
	v_and_b32_e32 v18, 0xffff0000, v18
	v_and_b32_e32 v19, 0xffff0000, v19
	v_mul_f32_e32 v20, v20, v20
	v_mul_f32_e32 v21, v21, v21
	v_fmac_f32_e32 v20, v18, v18
	v_fmac_f32_e32 v21, v19, v19
	v_add_f32_e32 v18, v20, v21
	s_waitcnt vmcnt(3)
	v_mov_b64_e32 v[14:15], v[32:33]
	v_mov_b64_e32 v[16:17], v[34:35]
	v_bfe_u32 v22, v14, 16, 1
	v_bfe_u32 v23, v15, 16, 1
	v_bfe_u32 v25, v17, 16, 1
	v_bfe_u32 v24, v16, 16, 1
	v_add3_u32 v22, v14, v22, s20
	v_add3_u32 v14, v15, v23, s20
	v_add3_u32 v15, v17, v25, s20
	v_add3_u32 v23, v16, v24, s20
	v_and_b32_e32 v24, 0xffff0000, v14
	v_and_b32_e32 v25, 0xffff0000, v15
	v_or_b32_sdwa v14, v24, v22 dst_sel:DWORD dst_unused:UNUSED_PAD src0_sel:DWORD src1_sel:WORD_1
	v_or_b32_sdwa v15, v25, v23 dst_sel:DWORD dst_unused:UNUSED_PAD src0_sel:DWORD src1_sel:WORD_1
	global_store_dwordx2 v2, v[14:15], s[10:11] offset:512
	v_and_b32_e32 v19, 0xffff0000, v22
	v_and_b32_e32 v20, 0xffff0000, v23
	v_mul_f32_e32 v21, v24, v24
	v_mul_f32_e32 v22, v25, v25
	v_fmac_f32_e32 v21, v19, v19
	v_fmac_f32_e32 v22, v20, v20
	v_add_f32_e32 v19, v21, v22
	v_add_f32_e32 v18, v18, v19
	s_waitcnt vmcnt(3)
	v_mov_b64_e32 v[14:15], v[36:37]
	v_mov_b64_e32 v[16:17], v[38:39]
	v_bfe_u32 v26, v14, 16, 1
	v_bfe_u32 v27, v15, 16, 1
	v_bfe_u32 v29, v17, 16, 1
	v_bfe_u32 v28, v16, 16, 1
	v_add3_u32 v26, v14, v26, s20
	v_add3_u32 v14, v15, v27, s20
	v_add3_u32 v15, v17, v29, s20
	v_add3_u32 v27, v16, v28, s20
	v_and_b32_e32 v28, 0xffff0000, v14
	v_and_b32_e32 v29, 0xffff0000, v15
	v_or_b32_sdwa v14, v28, v26 dst_sel:DWORD dst_unused:UNUSED_PAD src0_sel:DWORD src1_sel:WORD_1
	v_or_b32_sdwa v15, v29, v27 dst_sel:DWORD dst_unused:UNUSED_PAD src0_sel:DWORD src1_sel:WORD_1
	global_store_dwordx2 v2, v[14:15], s[10:11] offset:1024
	v_and_b32_e32 v19, 0xffff0000, v26
	v_and_b32_e32 v20, 0xffff0000, v27
	v_mul_f32_e32 v21, v28, v28
	v_mul_f32_e32 v22, v29, v29
	v_fmac_f32_e32 v21, v19, v19
	v_fmac_f32_e32 v22, v20, v20
	v_add_f32_e32 v19, v21, v22
	v_add_f32_e32 v18, v18, v19
	s_waitcnt vmcnt(3)
	v_mov_b64_e32 v[14:15], v[40:41]
	v_mov_b64_e32 v[16:17], v[42:43]
	v_bfe_u32 v20, v15, 16, 1
	v_bfe_u32 v22, v17, 16, 1
	v_bfe_u32 v19, v14, 16, 1
	v_bfe_u32 v21, v16, 16, 1
	v_add3_u32 v15, v15, v20, s20
	v_add3_u32 v17, v17, v22, s20
	v_add3_u32 v14, v14, v19, s20
	v_add3_u32 v16, v16, v21, s20
	v_and_b32_e32 v15, 0xffff0000, v15
	v_and_b32_e32 v17, 0xffff0000, v17
	v_and_b32_e32 v19, 0xffff0000, v14
	v_and_b32_e32 v20, 0xffff0000, v16
	v_mul_f32_e32 v21, v15, v15
	v_mul_f32_e32 v22, v17, v17
	v_fmac_f32_e32 v21, v19, v19
	v_fmac_f32_e32 v22, v20, v20
	v_add_f32_e32 v19, v21, v22
	v_add_f32_e32 v18, v18, v19
	ds_bpermute_b32 v19, v4, v18
	v_or_b32_sdwa v14, v15, v14 dst_sel:DWORD dst_unused:UNUSED_PAD src0_sel:DWORD src1_sel:WORD_1
	v_or_b32_sdwa v15, v17, v16 dst_sel:DWORD dst_unused:UNUSED_PAD src0_sel:DWORD src1_sel:WORD_1
	global_store_dwordx2 v2, v[14:15], s[10:11] offset:1536
	s_mov_b64 s[10:11], -1
	s_waitcnt lgkmcnt(0)
	v_add_f32_e32 v18, v18, v19
	ds_bpermute_b32 v19, v8, v18
	s_waitcnt lgkmcnt(0)
	v_add_f32_e32 v18, v18, v19
	ds_bpermute_b32 v19, v9, v18
	s_waitcnt lgkmcnt(0)
	v_add_f32_e32 v18, v18, v19
	ds_bpermute_b32 v19, v10, v18
	s_waitcnt lgkmcnt(0)
	v_add_f32_e32 v18, v18, v19
	ds_bpermute_b32 v19, v11, v18
	s_waitcnt lgkmcnt(0)
	v_add_f32_e32 v18, v18, v19
	ds_bpermute_b32 v19, v12, v18
	s_waitcnt lgkmcnt(0)
	v_add_f32_e32 v14, v18, v19
	s_cbranch_scc1 .LBB0_357
	s_andn2_b64 vcc, exec, s[10:11]
	s_cbranch_vccnz .LBB0_354
	s_branch .LBB0_360
